# saddr
# speedup vs baseline: 1.0070x; 1.0026x over previous
.Lpr2_nowrite:
	s_movk_i32 s4, 0x1a0
	v_add_u32_e32 v59, s29, v69
	v_cmp_gt_u32_e32 vcc, s4, v59
	v_add_f32_e32 v50, v78, v79
	v_lshlrev_b32_e32 v18, 2, v59
	s_and_saveexec_b64 s[0:1], vcc
	v_fma_f32 v50, v76, v50, -v77
	ds_write_b32 v18, v50 offset:41984
	s_or_b64 exec, exec, s[0:1]
	s_mov_b64 s[14:15], s[58:59]
	s_waitcnt lgkmcnt(0)
	v_mov_b32_e32 v18, 0xbfb8aa3b
	s_lshl_b32 s3, s21, 4
	s_cmpk_gt_i32 s20, 0x7fff
	v_cmp_gt_u32_e32 vcc, 32, v69
	s_waitcnt lgkmcnt(0)
	v_mul_f32_e32 v18, s34, v18
	v_exp_f32_e32 v70, v18
	v_mov_b32_e32 v18, 0
	v_and_b32_e32 v71, 48, v0
	s_mov_b32 s10, s20
	s_barrier
	s_cbranch_scc1 .LBB0_37
	s_sub_i32 s2, s20, s3
	s_add_i32 s9, s3, s20
	s_mov_b32 s4, 1.0
	s_mov_b32 s8, 0x3fb4c4be
	v_lshlrev_b32_e32 v72, 4, v69
	v_cmp_eq_u32_e64 s[0:1], 1, v1
	v_lshl_add_u32 v38, s2, 5, v69
	v_lshlrev_b32_e32 v38, 2, v38
	v_lshlrev_b32_e32 v39, 7, v68
	v_lshl_add_u32 v39, v1, 5, v39
	s_lshl_b32 s7, s21, 11
	v_mov_b32_e32 v18, 0
	s_mov_b32 s12, 0
	s_mov_b32 s2, 0x4a000000
	s_mov_b32 s5, s4
	s_mov_b32 s6, 0x3f34c4be
	v_mov_b64_e32 v[40:41], s[8:9]
	s_mov_b32 s8, 0x400a34e2
	s_mov_b32 s33, 0
	s_branch .LBB0_35
.LBB0_34:
	s_or_b64 exec, exec, s[10:11]
	ds_read_b128 v[18:21], v72
	s_waitcnt vmcnt(2)
	v_cvt_pk_f16_f32 v14, v14, v15
	v_cvt_pk_f16_f32 v15, v16, v17
	v_cvt_pk_f16_f32 v16, v10, v11
	ds_read_b128 v[22:25], v71 offset:41984
	v_cvt_pk_f16_f32 v17, v12, v13
	ds_read_b128 v[10:13], v72 offset:1024
	ds_read_b128 v[26:29], v71 offset:42048
	s_waitcnt vmcnt(0)
	v_cvt_pk_f16_f32 v0, v6, v7
	v_cvt_pk_f16_f32 v1, v8, v9
	v_cvt_pk_f16_f32 v2, v2, v3
	v_cvt_pk_f16_f32 v3, v4, v5
	s_waitcnt lgkmcnt(2)
	v_mfma_f32_16x16x32_f16 v[30:33], v[18:21], v[14:17], v[22:25]
	s_add_i32 s10, s20, s12
	v_mfma_f32_16x16x32_f16 v[18:21], v[18:21], v[0:3], v[22:25]
	ds_read_b128 v[4:7], v72 offset:2048
	s_nop 1
	ds_read_b128 v[22:25], v71 offset:42112
	s_waitcnt lgkmcnt(2)
	v_mfma_f32_16x16x32_f16 v[34:37], v[10:13], v[14:17], v[26:29]
	v_exp_f32_e32 v78, v30
	v_exp_f32_e32 v79, v31
	v_exp_f32_e32 v20, v20
	v_mfma_f32_16x16x32_f16 v[8:11], v[10:13], v[0:3], v[26:29]
	ds_read_b128 v[44:47], v71 offset:42176
	s_nop 2
	v_exp_f32_e64 v80, v34 clamp
	v_exp_f32_e64 v81, v35 clamp
	ds_read_b128 v[26:29], v72 offset:3072
	s_waitcnt lgkmcnt(2)
	v_mfma_f32_16x16x32_f16 v[48:51], v[4:7], v[14:17], v[22:25]
	v_exp_f32_e64 v82, v36 clamp
	v_exp_f32_e64 v83, v37 clamp
	v_exp_f32_e32 v21, v21
	v_mfma_f32_16x16x32_f16 v[22:25], v[4:7], v[0:3], v[22:25]
	ds_read_b128 v[52:55], v72 offset:4096
	ds_read_b128 v[56:59], v71 offset:42240
	s_nop 1
	v_exp_f32_e32 v4, v48
	s_waitcnt lgkmcnt(2)
	v_mfma_f32_16x16x32_f16 v[60:63], v[26:29], v[14:17], v[44:47]
	v_exp_f32_e32 v5, v49
	v_exp_f32_e32 v48, v32
	v_exp_f32_e32 v49, v33
	v_mfma_f32_16x16x32_f16 v[26:29], v[26:29], v[0:3], v[44:47]
	ds_read_b128 v[64:67], v71 offset:42304
	v_exp_f32_e32 v6, v50
	v_exp_f32_e32 v7, v51
	ds_read_b128 v[44:47], v72 offset:5120
	s_waitcnt lgkmcnt(2)
	v_mfma_f32_16x16x32_f16 v[74:77], v[52:55], v[14:17], v[56:59]
	v_exp_f32_e32 v50, v18
	v_exp_f32_e32 v51, v19
	v_exp_f32_e32 v26, v26
	v_mfma_f32_16x16x32_f16 v[30:33], v[52:55], v[0:3], v[56:59]
	v_exp_f32_e64 v52, v8 clamp
	v_exp_f32_e64 v53, v9 clamp
	v_exp_f32_e32 v8, v22
	s_waitcnt lgkmcnt(0)
	v_mfma_f32_16x16x32_f16 v[34:37], v[44:47], v[14:17], v[64:67]
	v_exp_f32_e32 v9, v23
	v_exp_f32_e64 v22, v10 clamp
	v_exp_f32_e64 v23, v11 clamp
	v_mfma_f32_16x16x32_f16 v[44:47], v[44:47], v[0:3], v[64:67]
	v_exp_f32_e32 v10, v24
	v_exp_f32_e32 v11, v25
	s_nop 1
	v_exp_f32_e32 v12, v34
	v_exp_f32_e32 v13, v35
	v_exp_f32_e32 v18, v36
	v_exp_f32_e32 v24, v60
	v_exp_f32_e32 v25, v61
	v_exp_f32_e64 v54, v74 clamp
	v_exp_f32_e64 v55, v75 clamp
	v_exp_f32_e32 v34, v62
	v_exp_f32_e32 v35, v63
	v_exp_f32_e64 v56, v76 clamp
	v_exp_f32_e64 v57, v77 clamp
	v_exp_f32_e32 v19, v37
	v_exp_f32_e32 v27, v27
	v_exp_f32_e64 v30, v30 clamp
	v_exp_f32_e64 v31, v31 clamp
	v_exp_f32_e32 v36, v44
	v_exp_f32_e32 v37, v45
	v_exp_f32_e32 v28, v28
	v_exp_f32_e32 v29, v29
	v_exp_f32_e64 v32, v32 clamp
	v_exp_f32_e64 v33, v33 clamp
	v_exp_f32_e32 v44, v46
	v_exp_f32_e32 v45, v47
	v_pk_fma_f32 v[58:59], v[80:81], s[2:3], 1.0 op_sel_hi:[1,0,0]
	v_pk_fma_f32 v[60:61], v[82:83], s[2:3], 1.0 op_sel_hi:[1,0,0]
	v_pk_fma_f32 v[52:53], v[52:53], s[2:3], 1.0 op_sel_hi:[1,0,0]
	v_pk_fma_f32 v[22:23], v[22:23], s[2:3], 1.0 op_sel_hi:[1,0,0]
	v_pk_fma_f32 v[54:55], v[54:55], s[2:3], 1.0 op_sel_hi:[1,0,0]
	v_pk_fma_f32 v[56:57], v[56:57], s[2:3], 1.0 op_sel_hi:[1,0,0]
	v_pk_fma_f32 v[30:31], v[30:31], s[2:3], 1.0 op_sel_hi:[1,0,0]
	v_pk_fma_f32 v[32:33], v[32:33], s[2:3], 1.0 op_sel_hi:[1,0,0]
	v_pk_fma_f32 v[46:47], v[78:79], v[58:59], v[58:59]
	v_pk_fma_f32 v[48:49], v[48:49], v[60:61], v[60:61]
	v_pk_fma_f32 v[50:51], v[50:51], v[52:53], v[52:53]
	v_pk_fma_f32 v[20:21], v[20:21], v[22:23], v[22:23]
	v_pk_fma_f32 v[24:25], v[24:25], v[54:55], v[54:55]
	v_pk_fma_f32 v[34:35], v[34:35], v[56:57], v[56:57]
	v_pk_fma_f32 v[26:27], v[26:27], v[30:31], v[30:31]
	v_pk_fma_f32 v[28:29], v[28:29], v[32:33], v[32:33]
	v_pk_fma_f32 v[58:59], v[58:59], s[6:7], v[40:41] op_sel_hi:[1,0,0] neg_lo:[1,0,0] neg_hi:[1,0,0]
	v_pk_fma_f32 v[60:61], v[60:61], s[6:7], v[40:41] op_sel_hi:[1,0,0] neg_lo:[1,0,0] neg_hi:[1,0,0]
	v_pk_fma_f32 v[52:53], v[52:53], s[6:7], v[40:41] op_sel_hi:[1,0,0] neg_lo:[1,0,0] neg_hi:[1,0,0]
	v_pk_fma_f32 v[22:23], v[22:23], s[6:7], v[40:41] op_sel_hi:[1,0,0] neg_lo:[1,0,0] neg_hi:[1,0,0]
	v_pk_fma_f32 v[54:55], v[54:55], s[6:7], v[40:41] op_sel_hi:[1,0,0] neg_lo:[1,0,0] neg_hi:[1,0,0]
	v_pk_fma_f32 v[56:57], v[56:57], s[6:7], v[40:41] op_sel_hi:[1,0,0] neg_lo:[1,0,0] neg_hi:[1,0,0]
	v_pk_fma_f32 v[30:31], v[30:31], s[6:7], v[40:41] op_sel_hi:[1,0,0] neg_lo:[1,0,0] neg_hi:[1,0,0]
	v_pk_fma_f32 v[32:33], v[32:33], s[6:7], v[40:41] op_sel_hi:[1,0,0] neg_lo:[1,0,0] neg_hi:[1,0,0]
	v_pk_fma_f32 v[46:47], v[4:5], v[46:47], v[46:47]
	v_pk_fma_f32 v[48:49], v[6:7], v[48:49], v[48:49]
	v_pk_fma_f32 v[50:51], v[8:9], v[50:51], v[50:51]
	v_pk_fma_f32 v[20:21], v[10:11], v[20:21], v[20:21]
	v_pk_fma_f32 v[24:25], v[12:13], v[24:25], v[24:25]
	v_pk_fma_f32 v[34:35], v[18:19], v[34:35], v[34:35]
	v_pk_fma_f32 v[26:27], v[36:37], v[26:27], v[26:27]
	v_pk_fma_f32 v[28:29], v[44:45], v[28:29], v[28:29]
	v_rcp_f32_e64 v46, v46 clamp
	v_rcp_f32_e64 v47, v47 clamp
	v_rcp_f32_e64 v48, v48 clamp
	v_rcp_f32_e64 v49, v49 clamp
	v_rcp_f32_e64 v50, v50 clamp
	v_rcp_f32_e64 v51, v51 clamp
	v_rcp_f32_e64 v20, v20 clamp
	v_rcp_f32_e64 v21, v21 clamp
	v_rcp_f32_e64 v24, v24 clamp
	v_rcp_f32_e64 v25, v25 clamp
	v_rcp_f32_e64 v34, v34 clamp
	v_rcp_f32_e64 v35, v35 clamp
	v_rcp_f32_e64 v26, v26 clamp
	v_rcp_f32_e64 v27, v27 clamp
	v_rcp_f32_e64 v28, v28 clamp
	v_rcp_f32_e64 v29, v29 clamp
	v_pk_mul_f32 v[46:47], v[58:59], v[46:47]
	v_pk_mul_f32 v[48:49], v[60:61], v[48:49]
	v_pk_mul_f32 v[50:51], v[52:53], v[50:51]
	v_pk_mul_f32 v[20:21], v[22:23], v[20:21]
	v_pk_mul_f32 v[22:23], v[54:55], v[24:25]
	v_pk_mul_f32 v[24:25], v[56:57], v[34:35]
	v_pk_mul_f32 v[26:27], v[30:31], v[26:27]
	v_pk_mul_f32 v[28:29], v[32:33], v[28:29]
	v_pk_fma_f32 v[4:5], v[4:5], v[46:47], v[46:47]
	v_pk_fma_f32 v[6:7], v[6:7], v[48:49], v[48:49]
	v_pk_fma_f32 v[8:9], v[8:9], v[50:51], v[50:51]
	v_pk_fma_f32 v[10:11], v[10:11], v[20:21], v[20:21]
	v_pk_fma_f32 v[12:13], v[12:13], v[22:23], v[22:23]
	v_pk_fma_f32 v[18:19], v[18:19], v[24:25], v[24:25]
	v_pk_fma_f32 v[30:31], v[36:37], v[26:27], v[26:27]
	v_pk_fma_f32 v[32:33], v[44:45], v[28:29], v[28:29]
	s_nop 0
	v_pk_fma_f32 v[4:5], v[4:5], v[4:5], s[4:5] neg_lo:[1,0,0] neg_hi:[1,0,0] clamp
	v_pk_fma_f32 v[6:7], v[6:7], v[6:7], s[4:5] neg_lo:[1,0,0] neg_hi:[1,0,0] clamp
	v_pk_fma_f32 v[8:9], v[8:9], v[8:9], s[4:5] neg_lo:[1,0,0] neg_hi:[1,0,0] clamp
	v_pk_fma_f32 v[10:11], v[10:11], v[10:11], s[4:5] neg_lo:[1,0,0] neg_hi:[1,0,0] clamp
	v_pk_fma_f32 v[12:13], v[12:13], v[12:13], s[4:5] neg_lo:[1,0,0] neg_hi:[1,0,0] clamp
	v_pk_fma_f32 v[18:19], v[18:19], v[18:19], s[4:5] neg_lo:[1,0,0] neg_hi:[1,0,0] clamp
	v_pk_fma_f32 v[30:31], v[30:31], v[30:31], s[4:5] neg_lo:[1,0,0] neg_hi:[1,0,0] clamp
	s_nop 0
	v_pk_fma_f32 v[32:33], v[32:33], v[32:33], s[4:5] neg_lo:[1,0,0] neg_hi:[1,0,0] clamp
	s_nop 0
	v_pk_fma_f32 v[8:9], v[8:9], v[8:9], s[8:9] op_sel_hi:[1,1,0]
	v_pk_fma_f32 v[10:11], v[10:11], v[10:11], s[8:9] op_sel_hi:[1,1,0]
	v_pk_fma_f32 v[12:13], v[12:13], v[12:13], s[8:9] op_sel_hi:[1,1,0]
	v_pk_fma_f32 v[18:19], v[18:19], v[18:19], s[8:9] op_sel_hi:[1,1,0]
	v_pk_fma_f32 v[32:33], v[32:33], v[32:33], s[8:9] op_sel_hi:[1,1,0]
	v_pk_fma_f32 v[4:5], v[4:5], v[4:5], s[8:9] op_sel_hi:[1,1,0]
	v_pk_fma_f32 v[6:7], v[6:7], v[6:7], s[8:9] op_sel_hi:[1,1,0]
	v_pk_fma_f32 v[30:31], v[30:31], v[30:31], s[8:9] op_sel_hi:[1,1,0]
	v_pk_mul_f32 v[8:9], v[50:51], v[8:9]
	v_pk_mul_f32 v[84:85], v[20:21], v[10:11]
	v_pk_mul_f32 v[86:87], v[22:23], v[12:13]
	v_pk_mul_f32 v[10:11], v[24:25], v[18:19]
	v_pk_mul_f32 v[12:13], v[28:29], v[32:33]
	v_pk_mul_f32 v[64:65], v[46:47], v[4:5]
	v_pk_mul_f32 v[82:83], v[48:49], v[6:7]
	v_pk_mul_f32 v[20:21], v[30:31], v[26:27]
	ds_read_b128 v[4:7], v72 offset:6144
	ds_read_b128 v[22:25], v71 offset:42368
	ds_read_b128 v[26:29], v72 offset:7168
	ds_read_b128 v[30:33], v71 offset:42432
	v_cvt_pk_f16_f32 v19, v84, v85
	v_cvt_pk_f16_f32 v18, v8, v9
	v_cvt_pk_f16_f32 v20, v20, v21
	v_cvt_pk_f16_f32 v21, v12, v13
	s_waitcnt lgkmcnt(2)
	v_mfma_f32_16x16x32_f16 v[34:37], v[4:7], v[14:17], v[22:25]
	v_mfma_f32_16x16x32_f16 v[44:47], v[4:7], v[0:3], v[22:25]
	ds_read_b128 v[4:7], v72 offset:8192
	ds_read_b128 v[48:51], v71 offset:42496
	s_waitcnt lgkmcnt(2)
	v_mfma_f32_16x16x32_f16 v[52:55], v[26:29], v[14:17], v[30:33]
	v_cvt_pk_f16_f32 v22, v64, v65
	v_cvt_pk_f16_f32 v23, v82, v83
	v_cvt_pk_f16_f32 v24, v86, v87
	v_mfma_f32_16x16x32_f16 v[26:29], v[26:29], v[0:3], v[30:33]
	ds_read_b128 v[56:59], v71 offset:42560
	v_exp_f32_e32 v86, v34
	v_exp_f32_e32 v87, v35
	ds_read_b128 v[30:33], v72 offset:9216
	s_waitcnt lgkmcnt(2)
	v_mfma_f32_16x16x32_f16 v[60:63], v[4:7], v[14:17], v[48:51]
	v_exp_f32_e64 v88, v52 clamp
	v_exp_f32_e64 v89, v53 clamp
	v_exp_f32_e64 v90, v54 clamp
	v_mfma_f32_16x16x32_f16 v[48:51], v[4:7], v[0:3], v[48:51]
	ds_read_b128 v[64:67], v72 offset:10240
	ds_read_b128 v[74:77], v71 offset:42624
	s_nop 1
	v_exp_f32_e32 v4, v60
	s_waitcnt lgkmcnt(2)
	v_mfma_f32_16x16x32_f16 v[78:81], v[30:33], v[14:17], v[56:59]
	v_exp_f32_e32 v5, v61
	v_exp_f32_e32 v60, v36
	v_exp_f32_e32 v61, v37
	v_mfma_f32_16x16x32_f16 v[30:33], v[30:33], v[0:3], v[56:59]
	ds_read_b128 v[82:85], v71 offset:42688
	v_exp_f32_e64 v91, v55 clamp
	v_exp_f32_e32 v6, v62
	ds_read_b128 v[56:59], v72 offset:11264
	s_waitcnt lgkmcnt(2)
	v_mfma_f32_16x16x32_f16 v[34:37], v[64:67], v[14:17], v[74:77]
	v_exp_f32_e32 v7, v63
	v_exp_f32_e32 v8, v48
	v_exp_f32_e32 v9, v49
	v_mfma_f32_16x16x32_f16 v[52:55], v[64:67], v[0:3], v[74:77]
	v_exp_f32_e32 v44, v44
	v_exp_f32_e32 v45, v45
	v_exp_f32_e64 v26, v26 clamp
	s_waitcnt lgkmcnt(0)
	v_mfma_f32_16x16x32_f16 v[14:17], v[56:59], v[14:17], v[82:85]
	v_exp_f32_e64 v27, v27 clamp
	v_exp_f32_e32 v46, v46
	v_exp_f32_e32 v47, v47
	v_mfma_f32_16x16x32_f16 v[56:59], v[56:59], v[0:3], v[82:85]
	v_exp_f32_e64 v28, v28 clamp
	s_nop 2
	v_exp_f32_e32 v2, v14
	v_exp_f32_e32 v3, v15
	v_exp_f32_e32 v14, v16
	v_exp_f32_e32 v15, v17
	v_exp_f32_e32 v16, v30
	v_exp_f32_e32 v17, v31
	v_exp_f32_e64 v29, v29 clamp
	v_exp_f32_e32 v0, v50
	v_exp_f32_e32 v1, v51
	v_exp_f32_e32 v48, v78
	v_exp_f32_e32 v49, v79
	v_exp_f32_e64 v34, v34 clamp
	v_exp_f32_e64 v35, v35 clamp
	v_exp_f32_e32 v50, v80
	v_exp_f32_e32 v51, v81
	v_exp_f32_e64 v36, v36 clamp
	v_exp_f32_e64 v37, v37 clamp
	v_exp_f32_e64 v30, v52 clamp
	v_exp_f32_e64 v31, v53 clamp
	v_exp_f32_e32 v52, v56
	v_exp_f32_e32 v53, v57
	v_exp_f32_e32 v32, v32
	v_exp_f32_e32 v33, v33
	v_exp_f32_e64 v54, v54 clamp
	v_exp_f32_e64 v55, v55 clamp
	v_exp_f32_e32 v56, v58
	v_cvt_pk_f16_f32 v25, v10, v11
	v_exp_f32_e32 v57, v59
	v_pk_fma_f32 v[30:31], v[30:31], s[2:3], 1.0 op_sel_hi:[1,0,0]
	v_pk_fma_f32 v[10:11], v[88:89], s[2:3], 1.0 op_sel_hi:[1,0,0]
	v_pk_fma_f32 v[12:13], v[90:91], s[2:3], 1.0 op_sel_hi:[1,0,0]
	v_pk_fma_f32 v[26:27], v[26:27], s[2:3], 1.0 op_sel_hi:[1,0,0]
	v_pk_fma_f32 v[28:29], v[28:29], s[2:3], 1.0 op_sel_hi:[1,0,0]
	v_pk_fma_f32 v[34:35], v[34:35], s[2:3], 1.0 op_sel_hi:[1,0,0]
	v_pk_fma_f32 v[36:37], v[36:37], s[2:3], 1.0 op_sel_hi:[1,0,0]
	v_pk_fma_f32 v[54:55], v[54:55], s[2:3], 1.0 op_sel_hi:[1,0,0]
	v_pk_fma_f32 v[16:17], v[16:17], v[30:31], v[30:31]
	v_pk_fma_f32 v[58:59], v[86:87], v[10:11], v[10:11]
	v_pk_fma_f32 v[10:11], v[10:11], s[6:7], v[40:41] op_sel_hi:[1,0,0] neg_lo:[1,0,0] neg_hi:[1,0,0]
	v_pk_fma_f32 v[60:61], v[60:61], v[12:13], v[12:13]
	v_pk_fma_f32 v[12:13], v[12:13], s[6:7], v[40:41] op_sel_hi:[1,0,0] neg_lo:[1,0,0] neg_hi:[1,0,0]
	v_pk_fma_f32 v[44:45], v[44:45], v[26:27], v[26:27]
	v_pk_fma_f32 v[46:47], v[46:47], v[28:29], v[28:29]
	v_pk_fma_f32 v[48:49], v[48:49], v[34:35], v[34:35]
	v_pk_fma_f32 v[50:51], v[50:51], v[36:37], v[36:37]
	v_pk_fma_f32 v[32:33], v[32:33], v[54:55], v[54:55]
	v_pk_fma_f32 v[16:17], v[52:53], v[16:17], v[16:17]
	v_pk_fma_f32 v[26:27], v[26:27], s[6:7], v[40:41] op_sel_hi:[1,0,0] neg_lo:[1,0,0] neg_hi:[1,0,0]
	v_pk_fma_f32 v[28:29], v[28:29], s[6:7], v[40:41] op_sel_hi:[1,0,0] neg_lo:[1,0,0] neg_hi:[1,0,0]
	v_pk_fma_f32 v[34:35], v[34:35], s[6:7], v[40:41] op_sel_hi:[1,0,0] neg_lo:[1,0,0] neg_hi:[1,0,0]
	v_pk_fma_f32 v[36:37], v[36:37], s[6:7], v[40:41] op_sel_hi:[1,0,0] neg_lo:[1,0,0] neg_hi:[1,0,0]
	v_pk_fma_f32 v[30:31], v[30:31], s[6:7], v[40:41] op_sel_hi:[1,0,0] neg_lo:[1,0,0] neg_hi:[1,0,0]
	v_pk_fma_f32 v[54:55], v[54:55], s[6:7], v[40:41] op_sel_hi:[1,0,0] neg_lo:[1,0,0] neg_hi:[1,0,0]
	v_pk_fma_f32 v[58:59], v[4:5], v[58:59], v[58:59]
	v_pk_fma_f32 v[60:61], v[6:7], v[60:61], v[60:61]
	v_pk_fma_f32 v[44:45], v[8:9], v[44:45], v[44:45]
	v_pk_fma_f32 v[46:47], v[0:1], v[46:47], v[46:47]
	v_pk_fma_f32 v[48:49], v[2:3], v[48:49], v[48:49]
	v_pk_fma_f32 v[50:51], v[14:15], v[50:51], v[50:51]
	v_pk_fma_f32 v[32:33], v[56:57], v[32:33], v[32:33]
	v_rcp_f32_e64 v16, v16 clamp
	v_rcp_f32_e64 v17, v17 clamp
	v_rcp_f32_e64 v58, v58 clamp
	v_rcp_f32_e64 v59, v59 clamp
	v_rcp_f32_e64 v60, v60 clamp
	v_rcp_f32_e64 v61, v61 clamp
	v_rcp_f32_e64 v44, v44 clamp
	v_rcp_f32_e64 v45, v45 clamp
	v_rcp_f32_e64 v46, v46 clamp
	v_rcp_f32_e64 v47, v47 clamp
	v_rcp_f32_e64 v48, v48 clamp
	v_rcp_f32_e64 v49, v49 clamp
	v_rcp_f32_e64 v50, v50 clamp
	v_rcp_f32_e64 v51, v51 clamp
	v_rcp_f32_e64 v32, v32 clamp
	v_rcp_f32_e64 v33, v33 clamp
	v_pk_mul_f32 v[10:11], v[10:11], v[58:59]
	v_pk_mul_f32 v[12:13], v[12:13], v[60:61]
	v_pk_mul_f32 v[26:27], v[26:27], v[44:45]
	v_pk_mul_f32 v[34:35], v[34:35], v[48:49]
	v_pk_mul_f32 v[36:37], v[36:37], v[50:51]
	v_pk_mul_f32 v[28:29], v[28:29], v[46:47]
	v_pk_mul_f32 v[16:17], v[30:31], v[16:17]
	v_pk_mul_f32 v[30:31], v[54:55], v[32:33]
	v_pk_fma_f32 v[4:5], v[4:5], v[10:11], v[10:11]
	v_pk_fma_f32 v[6:7], v[6:7], v[12:13], v[12:13]
	v_pk_fma_f32 v[8:9], v[8:9], v[26:27], v[26:27]
	v_pk_fma_f32 v[2:3], v[2:3], v[34:35], v[34:35]
	v_pk_fma_f32 v[14:15], v[14:15], v[36:37], v[36:37]
	v_pk_fma_f32 v[0:1], v[0:1], v[28:29], v[28:29]
	v_pk_fma_f32 v[32:33], v[52:53], v[16:17], v[16:17]
	v_pk_fma_f32 v[44:45], v[56:57], v[30:31], v[30:31]
	s_nop 0
	v_pk_fma_f32 v[4:5], v[4:5], v[4:5], s[4:5] neg_lo:[1,0,0] neg_hi:[1,0,0] clamp
	v_pk_fma_f32 v[6:7], v[6:7], v[6:7], s[4:5] neg_lo:[1,0,0] neg_hi:[1,0,0] clamp
	v_pk_fma_f32 v[8:9], v[8:9], v[8:9], s[4:5] neg_lo:[1,0,0] neg_hi:[1,0,0] clamp
	v_pk_fma_f32 v[0:1], v[0:1], v[0:1], s[4:5] neg_lo:[1,0,0] neg_hi:[1,0,0] clamp
	v_pk_fma_f32 v[2:3], v[2:3], v[2:3], s[4:5] neg_lo:[1,0,0] neg_hi:[1,0,0] clamp
	v_pk_fma_f32 v[14:15], v[14:15], v[14:15], s[4:5] neg_lo:[1,0,0] neg_hi:[1,0,0] clamp
	v_pk_fma_f32 v[32:33], v[32:33], v[32:33], s[4:5] neg_lo:[1,0,0] neg_hi:[1,0,0] clamp
	s_nop 0
	v_pk_fma_f32 v[44:45], v[44:45], v[44:45], s[4:5] neg_lo:[1,0,0] neg_hi:[1,0,0] clamp
	s_nop 0
	v_pk_fma_f32 v[32:33], v[32:33], v[32:33], s[8:9] op_sel_hi:[1,1,0]
	v_pk_fma_f32 v[4:5], v[4:5], v[4:5], s[8:9] op_sel_hi:[1,1,0]
	v_pk_fma_f32 v[6:7], v[6:7], v[6:7], s[8:9] op_sel_hi:[1,1,0]
	v_pk_fma_f32 v[8:9], v[8:9], v[8:9], s[8:9] op_sel_hi:[1,1,0]
	v_pk_fma_f32 v[0:1], v[0:1], v[0:1], s[8:9] op_sel_hi:[1,1,0]
	v_pk_fma_f32 v[2:3], v[2:3], v[2:3], s[8:9] op_sel_hi:[1,1,0]
	v_pk_fma_f32 v[14:15], v[14:15], v[14:15], s[8:9] op_sel_hi:[1,1,0]
	v_pk_fma_f32 v[44:45], v[44:45], v[44:45], s[8:9] op_sel_hi:[1,1,0]
	v_pk_mul_f32 v[16:17], v[32:33], v[16:17]
	v_pk_mul_f32 v[52:53], v[10:11], v[4:5]
	v_pk_mul_f32 v[54:55], v[12:13], v[6:7]
	v_pk_mul_f32 v[26:27], v[26:27], v[8:9]
	v_pk_mul_f32 v[28:29], v[28:29], v[0:1]
	v_pk_mul_f32 v[56:57], v[34:35], v[2:3]
	v_pk_mul_f32 v[58:59], v[36:37], v[14:15]
	v_pk_mul_f32 v[60:61], v[30:31], v[44:45]
	ds_read_b128 v[0:3], v72 offset:12288
	ds_read_b128 v[4:7], v71 offset:42752
	ds_read_b128 v[8:11], v72 offset:13312
	ds_read_b128 v[12:15], v72 offset:14336
	ds_read_b128 v[34:37], v72 offset:15360
	ds_read_b128 v[44:47], v71 offset:42816
	v_cvt_pk_f16_f32 v30, v52, v53
	v_cvt_pk_f16_f32 v26, v26, v27
	v_cvt_pk_f16_f32 v31, v54, v55
	s_waitcnt lgkmcnt(4)
	v_mfma_f32_16x16x32_f16 v[48:51], v[0:3], v[22:25], v[4:7]
	v_cvt_pk_f16_f32 v32, v56, v57
	v_cvt_pk_f16_f32 v33, v58, v59
	v_cvt_pk_f16_f32 v27, v28, v29
	v_mfma_f32_16x16x32_f16 v[0:3], v[0:3], v[18:21], v[4:7]
	v_cvt_pk_f16_f32 v28, v16, v17
	v_cvt_pk_f16_f32 v29, v60, v61
	s_add_i32 s11, s9, s12
	s_waitcnt lgkmcnt(3)
	v_mfma_f32_16x16x32_f16 v[48:51], v[8:11], v[30:33], v[48:51]
	s_cmp_lt_i32 s11, 0x8000
	s_cselect_b32 s10, s11, s10
	s_ashr_i32 s11, s10, 31
	v_mfma_f32_16x16x32_f16 v[52:55], v[8:11], v[26:29], v[0:3]
	ds_read_b128 v[4:7], v72 offset:17408
	ds_read_b128 v[8:11], v71 offset:42880
	s_lshl_b64 s[10:11], s[10:11], 12
	s_add_u32 s10, s10, s36
	s_addc_u32 s11, s11, s37
	ds_read_b128 v[0:3], v72 offset:16384
	s_waitcnt lgkmcnt(3)
	v_mfma_f32_16x16x32_f16 v[56:59], v[12:15], v[22:25], v[44:47]
	v_exp_f32_e32 v106, v48
	v_exp_f32_e32 v107, v49
	v_exp_f32_e32 v110, v50
	v_mfma_f32_16x16x32_f16 v[12:15], v[12:15], v[18:21], v[44:47]
	v_exp_f32_e32 v111, v51
	v_exp_f32_e32 v114, v52
	v_exp_f32_e32 v115, v53
	v_mfma_f32_16x16x32_f16 v[44:47], v[34:37], v[30:33], v[56:59]
	v_mfma_f32_16x16x32_f16 v[56:59], v[34:37], v[26:29], v[12:15]
	ds_read_b128 v[34:37], v72 offset:19456
	ds_read_b128 v[60:63], v71 offset:42944
	s_nop 4
	v_exp_f32_e64 v108, v44 clamp
	ds_read_b128 v[12:15], v72 offset:18432
	s_waitcnt lgkmcnt(3)
	v_mfma_f32_16x16x32_f16 v[64:67], v[0:3], v[22:25], v[8:11]
	v_exp_f32_e64 v109, v45 clamp
	v_exp_f32_e64 v112, v46 clamp
	v_exp_f32_e64 v113, v47 clamp
	v_mfma_f32_16x16x32_f16 v[0:3], v[0:3], v[18:21], v[8:11]
	v_exp_f32_e64 v116, v56 clamp
	v_exp_f32_e64 v117, v57 clamp
	v_exp_f32_e64 v58, v58 clamp
	v_mfma_f32_16x16x32_f16 v[64:67], v[4:7], v[30:33], v[64:67]
	v_exp_f32_e64 v59, v59 clamp
	v_mfma_f32_16x16x32_f16 v[74:77], v[4:7], v[26:29], v[0:3]
	ds_read_b128 v[78:81], v72 offset:20480
	ds_read_b128 v[82:85], v72 offset:21504
	ds_read_b128 v[86:89], v71 offset:43008
	s_waitcnt lgkmcnt(3)
	v_mfma_f32_16x16x32_f16 v[6:9], v[12:15], v[22:25], v[60:63]
	v_mfma_f32_16x16x32_f16 v[60:63], v[12:15], v[18:21], v[60:63]
	global_load_dwordx4 v[10:13], v39, s[10:11] offset:16
	global_load_dwordx4 v[14:17], v39, s[10:11]
	global_load_dwordx4 v[2:5], v39, s[10:11] offset:2064
	v_mfma_f32_16x16x32_f16 v[90:93], v[34:37], v[30:33], v[6:9]
	v_mfma_f32_16x16x32_f16 v[60:63], v[34:37], v[26:29], v[60:63]
	s_nop 1
	global_load_dwordx4 v[6:9], v39, s[10:11] offset:2048
	ds_read_b128 v[94:97], v72 offset:22528
	ds_read_b128 v[98:101], v72 offset:23552
	ds_read_b128 v[102:105], v71 offset:43072
	s_waitcnt lgkmcnt(3)
	v_mfma_f32_16x16x32_f16 v[44:47], v[78:81], v[22:25], v[86:89]
	v_exp_f32_e32 v0, v64
	v_exp_f32_e32 v1, v65
	v_exp_f32_e32 v34, v66
	v_mfma_f32_16x16x32_f16 v[48:51], v[78:81], v[18:21], v[86:89]
	v_exp_f32_e32 v35, v67
	v_exp_f32_e32 v36, v74
	v_exp_f32_e32 v37, v75
	v_mfma_f32_16x16x32_f16 v[64:67], v[82:85], v[30:33], v[44:47]
	v_exp_f32_e32 v74, v54
	v_exp_f32_e32 v75, v55
	v_exp_f32_e32 v78, v92
	v_mfma_f32_16x16x32_f16 v[50:53], v[82:85], v[26:29], v[48:51]
	v_exp_f32_e32 v44, v76
	v_exp_f32_e32 v45, v77
	v_exp_f32_e32 v76, v90
	s_waitcnt lgkmcnt(0)
	v_mfma_f32_16x16x32_f16 v[46:49], v[94:97], v[22:25], v[102:105]
	v_exp_f32_e32 v77, v91
	v_exp_f32_e64 v64, v64 clamp
	v_exp_f32_e64 v65, v65 clamp
	v_mfma_f32_16x16x32_f16 v[54:57], v[94:97], v[18:21], v[102:105]
	v_exp_f32_e32 v79, v93
	v_exp_f32_e64 v66, v66 clamp
	v_exp_f32_e64 v67, v67 clamp
	v_mfma_f32_16x16x32_f16 v[46:49], v[98:101], v[30:33], v[46:49]
	v_exp_f32_e32 v60, v60
	v_exp_f32_e32 v61, v61
	v_exp_f32_e64 v50, v50 clamp
	v_mfma_f32_16x16x32_f16 v[54:57], v[98:101], v[26:29], v[54:57]
	v_exp_f32_e64 v51, v51 clamp
	s_nop 2
	v_exp_f32_e32 v46, v46
	v_exp_f32_e32 v47, v47
	v_exp_f32_e32 v48, v48
	v_exp_f32_e32 v49, v49
	v_exp_f32_e32 v54, v54
	v_exp_f32_e32 v55, v55
	v_exp_f32_e32 v62, v62
	v_exp_f32_e32 v63, v63
	v_exp_f32_e64 v52, v52 clamp
	v_exp_f32_e64 v53, v53 clamp
	v_exp_f32_e32 v56, v56
	v_exp_f32_e32 v57, v57
	v_pk_fma_f32 v[80:81], v[108:109], s[2:3], 1.0 op_sel_hi:[1,0,0]
	v_pk_fma_f32 v[82:83], v[112:113], s[2:3], 1.0 op_sel_hi:[1,0,0]
	v_pk_fma_f32 v[84:85], v[116:117], s[2:3], 1.0 op_sel_hi:[1,0,0]
	v_pk_fma_f32 v[58:59], v[58:59], s[2:3], 1.0 op_sel_hi:[1,0,0]
	v_pk_fma_f32 v[64:65], v[64:65], s[2:3], 1.0 op_sel_hi:[1,0,0]
	v_pk_fma_f32 v[66:67], v[66:67], s[2:3], 1.0 op_sel_hi:[1,0,0]
	v_pk_fma_f32 v[50:51], v[50:51], s[2:3], 1.0 op_sel_hi:[1,0,0]
	v_pk_fma_f32 v[52:53], v[52:53], s[2:3], 1.0 op_sel_hi:[1,0,0]
	v_pk_fma_f32 v[86:87], v[106:107], v[80:81], v[80:81]
	v_pk_fma_f32 v[88:89], v[110:111], v[82:83], v[82:83]
	v_pk_fma_f32 v[90:91], v[114:115], v[84:85], v[84:85]
	v_pk_fma_f32 v[74:75], v[74:75], v[58:59], v[58:59]
	v_pk_fma_f32 v[76:77], v[76:77], v[64:65], v[64:65]
	v_pk_fma_f32 v[78:79], v[78:79], v[66:67], v[66:67]
	v_pk_fma_f32 v[60:61], v[60:61], v[50:51], v[50:51]
	v_pk_fma_f32 v[62:63], v[62:63], v[52:53], v[52:53]
	v_pk_fma_f32 v[80:81], v[80:81], s[6:7], v[40:41] op_sel_hi:[1,0,0] neg_lo:[1,0,0] neg_hi:[1,0,0]
	v_pk_fma_f32 v[82:83], v[82:83], s[6:7], v[40:41] op_sel_hi:[1,0,0] neg_lo:[1,0,0] neg_hi:[1,0,0]
	v_pk_fma_f32 v[84:85], v[84:85], s[6:7], v[40:41] op_sel_hi:[1,0,0] neg_lo:[1,0,0] neg_hi:[1,0,0]
	v_pk_fma_f32 v[58:59], v[58:59], s[6:7], v[40:41] op_sel_hi:[1,0,0] neg_lo:[1,0,0] neg_hi:[1,0,0]
	v_pk_fma_f32 v[64:65], v[64:65], s[6:7], v[40:41] op_sel_hi:[1,0,0] neg_lo:[1,0,0] neg_hi:[1,0,0]
	v_pk_fma_f32 v[66:67], v[66:67], s[6:7], v[40:41] op_sel_hi:[1,0,0] neg_lo:[1,0,0] neg_hi:[1,0,0]
	v_pk_fma_f32 v[50:51], v[50:51], s[6:7], v[40:41] op_sel_hi:[1,0,0] neg_lo:[1,0,0] neg_hi:[1,0,0]
	v_pk_fma_f32 v[52:53], v[52:53], s[6:7], v[40:41] op_sel_hi:[1,0,0] neg_lo:[1,0,0] neg_hi:[1,0,0]
	v_pk_fma_f32 v[86:87], v[0:1], v[86:87], v[86:87]
	v_pk_fma_f32 v[88:89], v[34:35], v[88:89], v[88:89]
	v_pk_fma_f32 v[90:91], v[36:37], v[90:91], v[90:91]
	v_pk_fma_f32 v[74:75], v[44:45], v[74:75], v[74:75]
	v_pk_fma_f32 v[76:77], v[46:47], v[76:77], v[76:77]
	v_pk_fma_f32 v[78:79], v[48:49], v[78:79], v[78:79]
	v_pk_fma_f32 v[60:61], v[54:55], v[60:61], v[60:61]
	v_pk_fma_f32 v[62:63], v[56:57], v[62:63], v[62:63]
	v_rcp_f32_e64 v86, v86 clamp
	v_rcp_f32_e64 v87, v87 clamp
	v_rcp_f32_e64 v88, v88 clamp
	v_rcp_f32_e64 v89, v89 clamp
	v_rcp_f32_e64 v90, v90 clamp
	v_rcp_f32_e64 v91, v91 clamp
	v_rcp_f32_e64 v74, v74 clamp
	v_rcp_f32_e64 v75, v75 clamp
	v_rcp_f32_e64 v76, v76 clamp
	v_rcp_f32_e64 v77, v77 clamp
	v_rcp_f32_e64 v78, v78 clamp
	v_rcp_f32_e64 v79, v79 clamp
	v_rcp_f32_e64 v60, v60 clamp
	v_rcp_f32_e64 v61, v61 clamp
	v_rcp_f32_e64 v62, v62 clamp
	v_rcp_f32_e64 v63, v63 clamp
	v_pk_mul_f32 v[80:81], v[80:81], v[86:87]
	v_pk_mul_f32 v[82:83], v[82:83], v[88:89]
	v_pk_mul_f32 v[84:85], v[84:85], v[90:91]
	v_pk_mul_f32 v[58:59], v[58:59], v[74:75]
	v_pk_mul_f32 v[64:65], v[64:65], v[76:77]
	v_pk_mul_f32 v[66:67], v[66:67], v[78:79]
	v_pk_mul_f32 v[50:51], v[50:51], v[60:61]
	v_pk_mul_f32 v[60:61], v[52:53], v[62:63]
	v_pk_fma_f32 v[0:1], v[0:1], v[80:81], v[80:81]
	v_pk_fma_f32 v[34:35], v[34:35], v[82:83], v[82:83]
	v_pk_fma_f32 v[36:37], v[36:37], v[84:85], v[84:85]
	v_pk_fma_f32 v[44:45], v[44:45], v[58:59], v[58:59]
	v_pk_fma_f32 v[46:47], v[46:47], v[64:65], v[64:65]
	v_pk_fma_f32 v[48:49], v[48:49], v[66:67], v[66:67]
	v_pk_fma_f32 v[52:53], v[54:55], v[50:51], v[50:51]
	v_pk_fma_f32 v[54:55], v[56:57], v[60:61], v[60:61]
	s_nop 0
	v_pk_fma_f32 v[0:1], v[0:1], v[0:1], s[4:5] neg_lo:[1,0,0] neg_hi:[1,0,0] clamp
	v_pk_fma_f32 v[34:35], v[34:35], v[34:35], s[4:5] neg_lo:[1,0,0] neg_hi:[1,0,0] clamp
	v_pk_fma_f32 v[36:37], v[36:37], v[36:37], s[4:5] neg_lo:[1,0,0] neg_hi:[1,0,0] clamp
	v_pk_fma_f32 v[44:45], v[44:45], v[44:45], s[4:5] neg_lo:[1,0,0] neg_hi:[1,0,0] clamp
	v_pk_fma_f32 v[46:47], v[46:47], v[46:47], s[4:5] neg_lo:[1,0,0] neg_hi:[1,0,0] clamp
	v_pk_fma_f32 v[48:49], v[48:49], v[48:49], s[4:5] neg_lo:[1,0,0] neg_hi:[1,0,0] clamp
	v_pk_fma_f32 v[52:53], v[52:53], v[52:53], s[4:5] neg_lo:[1,0,0] neg_hi:[1,0,0] clamp
	s_nop 0
	v_pk_fma_f32 v[54:55], v[54:55], v[54:55], s[4:5] neg_lo:[1,0,0] neg_hi:[1,0,0] clamp
	s_nop 0
	v_pk_fma_f32 v[0:1], v[0:1], v[0:1], s[8:9] op_sel_hi:[1,1,0]
	v_pk_fma_f32 v[56:57], v[34:35], v[34:35], s[8:9] op_sel_hi:[1,1,0]
	v_pk_fma_f32 v[36:37], v[36:37], v[36:37], s[8:9] op_sel_hi:[1,1,0]
	v_pk_fma_f32 v[44:45], v[44:45], v[44:45], s[8:9] op_sel_hi:[1,1,0]
	v_pk_fma_f32 v[46:47], v[46:47], v[46:47], s[8:9] op_sel_hi:[1,1,0]
	v_pk_fma_f32 v[48:49], v[48:49], v[48:49], s[8:9] op_sel_hi:[1,1,0]
	v_pk_fma_f32 v[62:63], v[52:53], v[52:53], s[8:9] op_sel_hi:[1,1,0]
	v_pk_fma_f32 v[74:75], v[54:55], v[54:55], s[8:9] op_sel_hi:[1,1,0]
	v_pk_mul_f32 v[34:35], v[80:81], v[0:1]
	v_pk_mul_f32 v[56:57], v[82:83], v[56:57]
	v_pk_mul_f32 v[36:37], v[84:85], v[36:37]
	v_pk_mul_f32 v[52:53], v[58:59], v[44:45]
	v_pk_mul_f32 v[54:55], v[64:65], v[46:47]
	v_pk_mul_f32 v[0:1], v[66:67], v[48:49]
	v_pk_mul_f32 v[46:47], v[62:63], v[50:51]
	v_pk_mul_f32 v[44:45], v[60:61], v[74:75]
	ds_read_b128 v[48:51], v72 offset:24576
	ds_read_b128 v[58:61], v71 offset:43136
	ds_read_b128 v[62:65], v72 offset:25600
	ds_read_b128 v[74:77], v72 offset:26624
	ds_read_b128 v[78:81], v72 offset:27648
	ds_read_b128 v[82:85], v71 offset:43200
	v_cvt_pk_f16_f32 v34, v34, v35
	v_cvt_pk_f16_f32 v35, v56, v57
	s_waitcnt lgkmcnt(4)
	v_mfma_f32_16x16x32_f16 v[86:89], v[48:51], v[22:25], v[58:61]
	v_mfma_f32_16x16x32_f16 v[48:51], v[48:51], v[18:21], v[58:61]
	s_waitcnt lgkmcnt(3)
	v_mfma_f32_16x16x32_f16 v[58:61], v[62:65], v[30:33], v[86:89]
	v_mfma_f32_16x16x32_f16 v[86:89], v[62:65], v[26:29], v[48:51]
	ds_read_b128 v[62:65], v72 offset:29696
	ds_read_b128 v[90:93], v71 offset:43264
	s_nop 2
	ds_read_b128 v[48:51], v72 offset:28672
	s_waitcnt lgkmcnt(3)
	v_mfma_f32_16x16x32_f16 v[94:97], v[74:77], v[22:25], v[82:85]
	v_exp_f32_e32 v120, v86
	v_exp_f32_e32 v121, v87
	v_exp_f32_e32 v122, v88
	v_mfma_f32_16x16x32_f16 v[74:77], v[74:77], v[18:21], v[82:85]
	v_exp_f32_e32 v123, v89
	v_mfma_f32_16x16x32_f16 v[82:85], v[78:81], v[30:33], v[94:97]
	v_mfma_f32_16x16x32_f16 v[74:77], v[78:81], v[26:29], v[74:77]
	ds_read_b128 v[78:81], v72 offset:30720
	s_nop 0
	ds_read_b128 v[94:97], v72 offset:31744
	ds_read_b128 v[98:101], v71 offset:43328
	s_waitcnt lgkmcnt(3)
	v_mfma_f32_16x16x32_f16 v[102:105], v[48:51], v[22:25], v[90:93]
	s_nop 0
	v_exp_f32_e64 v66, v82 clamp
	v_exp_f32_e64 v67, v83 clamp
	v_exp_f32_e64 v118, v84 clamp
	v_mfma_f32_16x16x32_f16 v[48:51], v[48:51], v[18:21], v[90:93]
	v_exp_f32_e64 v119, v85 clamp
	v_exp_f32_e64 v124, v74 clamp
	v_exp_f32_e64 v125, v75 clamp
	v_mfma_f32_16x16x32_f16 v[90:93], v[62:65], v[30:33], v[102:105]
	v_exp_f32_e64 v126, v76 clamp
	v_exp_f32_e64 v127, v77 clamp
	v_mfma_f32_16x16x32_f16 v[102:105], v[62:65], v[26:29], v[48:51]
	ds_read_b128 v[106:109], v72 offset:32768
	ds_read_b128 v[110:113], v72 offset:33792
	v_exp_f32_e32 v62, v58
	v_exp_f32_e32 v63, v59
	v_exp_f32_e32 v64, v60
	v_exp_f32_e32 v65, v61
	ds_read_b128 v[114:117], v71 offset:43392
	s_waitcnt lgkmcnt(3)
	v_mfma_f32_16x16x32_f16 v[58:61], v[78:81], v[22:25], v[98:101]
	v_exp_f32_e32 v48, v90
	v_exp_f32_e32 v49, v91
	v_exp_f32_e32 v50, v92
	v_mfma_f32_16x16x32_f16 v[78:81], v[78:81], v[18:21], v[98:101]
	v_exp_f32_e32 v51, v93
	v_mfma_f32_16x16x32_f16 v[82:85], v[94:97], v[30:33], v[58:61]
	v_mfma_f32_16x16x32_f16 v[78:81], v[94:97], v[26:29], v[78:81]
	ds_read_b128 v[86:89], v72 offset:34816
	ds_read_b128 v[90:93], v72 offset:35840
	ds_read_b128 v[94:97], v71 offset:43456
	s_waitcnt lgkmcnt(3)
	v_mfma_f32_16x16x32_f16 v[74:77], v[106:109], v[22:25], v[114:117]
	v_exp_f32_e32 v58, v102
	v_exp_f32_e32 v59, v103
	v_exp_f32_e32 v60, v104
	v_mfma_f32_16x16x32_f16 v[98:101], v[106:109], v[18:21], v[114:117]
	v_exp_f32_e32 v61, v105
	v_exp_f32_e32 v102, v82
	v_exp_f32_e32 v103, v83
	v_exp_f32_e32 v104, v84
	v_exp_f32_e32 v105, v85
	v_mfma_f32_16x16x32_f16 v[74:77], v[110:113], v[30:33], v[74:77]
	v_mfma_f32_16x16x32_f16 v[82:85], v[110:113], v[26:29], v[98:101]
	s_waitcnt lgkmcnt(0)
	v_mfma_f32_16x16x32_f16 v[18:21], v[86:89], v[18:21], v[94:97]
	s_nop 4
	v_exp_f32_e64 v106, v74 clamp
	v_exp_f32_e64 v107, v75 clamp
	v_exp_f32_e64 v108, v76 clamp
	v_exp_f32_e64 v109, v77 clamp
	v_mfma_f32_16x16x32_f16 v[74:77], v[86:89], v[22:25], v[94:97]
	v_cvt_pk_f16_f32 v22, v36, v37
	v_cvt_pk_f16_f32 v23, v52, v53
	v_cvt_pk_f16_f32 v36, v54, v55
	v_mfma_f32_16x16x32_f16 v[18:21], v[90:93], v[26:29], v[18:21]
	v_exp_f32_e32 v52, v78
	v_exp_f32_e32 v53, v79
	v_exp_f32_e64 v54, v82 clamp
	v_mfma_f32_16x16x32_f16 v[30:33], v[90:93], v[30:33], v[74:77]
	v_exp_f32_e64 v55, v83 clamp
	s_nop 2
	v_exp_f32_e32 v18, v18
	v_exp_f32_e32 v19, v19
	v_exp_f32_e32 v26, v80
	v_exp_f32_e32 v27, v81
	v_exp_f32_e32 v30, v30
	v_exp_f32_e32 v31, v31
	v_exp_f32_e32 v32, v32
	v_exp_f32_e32 v33, v33
	v_exp_f32_e64 v28, v84 clamp
	v_exp_f32_e64 v29, v85 clamp
	v_exp_f32_e32 v20, v20
	v_cvt_pk_f16_f32 v24, v46, v47
	v_cvt_pk_f16_f32 v37, v0, v1
	v_cvt_pk_f16_f32 v25, v44, v45
	v_exp_f32_e32 v21, v21
	v_pk_fma_f32 v[0:1], v[66:67], s[2:3], 1.0 op_sel_hi:[1,0,0]
	v_pk_fma_f32 v[44:45], v[118:119], s[2:3], 1.0 op_sel_hi:[1,0,0]
	v_pk_fma_f32 v[46:47], v[124:125], s[2:3], 1.0 op_sel_hi:[1,0,0]
	v_pk_fma_f32 v[56:57], v[126:127], s[2:3], 1.0 op_sel_hi:[1,0,0]
	v_pk_fma_f32 v[66:67], v[106:107], s[2:3], 1.0 op_sel_hi:[1,0,0]
	v_pk_fma_f32 v[74:75], v[108:109], s[2:3], 1.0 op_sel_hi:[1,0,0]
	v_pk_fma_f32 v[54:55], v[54:55], s[2:3], 1.0 op_sel_hi:[1,0,0]
	v_pk_fma_f32 v[28:29], v[28:29], s[2:3], 1.0 op_sel_hi:[1,0,0]
	v_pk_fma_f32 v[62:63], v[62:63], v[0:1], v[0:1]
	v_pk_fma_f32 v[64:65], v[64:65], v[44:45], v[44:45]
	v_pk_fma_f32 v[76:77], v[120:121], v[46:47], v[46:47]
	v_pk_fma_f32 v[78:79], v[122:123], v[56:57], v[56:57]
	v_pk_fma_f32 v[80:81], v[102:103], v[66:67], v[66:67]
	v_pk_fma_f32 v[82:83], v[104:105], v[74:75], v[74:75]
	v_pk_fma_f32 v[52:53], v[52:53], v[54:55], v[54:55]
	v_pk_fma_f32 v[26:27], v[26:27], v[28:29], v[28:29]
	v_pk_fma_f32 v[0:1], v[0:1], s[6:7], v[40:41] op_sel_hi:[1,0,0] neg_lo:[1,0,0] neg_hi:[1,0,0]
	v_pk_fma_f32 v[44:45], v[44:45], s[6:7], v[40:41] op_sel_hi:[1,0,0] neg_lo:[1,0,0] neg_hi:[1,0,0]
	v_pk_fma_f32 v[46:47], v[46:47], s[6:7], v[40:41] op_sel_hi:[1,0,0] neg_lo:[1,0,0] neg_hi:[1,0,0]
	v_pk_fma_f32 v[56:57], v[56:57], s[6:7], v[40:41] op_sel_hi:[1,0,0] neg_lo:[1,0,0] neg_hi:[1,0,0]
	v_pk_fma_f32 v[66:67], v[66:67], s[6:7], v[40:41] op_sel_hi:[1,0,0] neg_lo:[1,0,0] neg_hi:[1,0,0]
	v_pk_fma_f32 v[74:75], v[74:75], s[6:7], v[40:41] op_sel_hi:[1,0,0] neg_lo:[1,0,0] neg_hi:[1,0,0]
	v_pk_fma_f32 v[54:55], v[54:55], s[6:7], v[40:41] op_sel_hi:[1,0,0] neg_lo:[1,0,0] neg_hi:[1,0,0]
	v_pk_fma_f32 v[28:29], v[28:29], s[6:7], v[40:41] op_sel_hi:[1,0,0] neg_lo:[1,0,0] neg_hi:[1,0,0]
	v_pk_fma_f32 v[62:63], v[48:49], v[62:63], v[62:63]
	v_pk_fma_f32 v[64:65], v[50:51], v[64:65], v[64:65]
	v_pk_fma_f32 v[76:77], v[58:59], v[76:77], v[76:77]
	v_pk_fma_f32 v[78:79], v[60:61], v[78:79], v[78:79]
	v_pk_fma_f32 v[80:81], v[30:31], v[80:81], v[80:81]
	v_pk_fma_f32 v[82:83], v[32:33], v[82:83], v[82:83]
	v_pk_fma_f32 v[52:53], v[18:19], v[52:53], v[52:53]
	v_pk_fma_f32 v[26:27], v[20:21], v[26:27], v[26:27]
	v_rcp_f32_e64 v62, v62 clamp
	v_rcp_f32_e64 v63, v63 clamp
	v_rcp_f32_e64 v64, v64 clamp
	v_rcp_f32_e64 v65, v65 clamp
	v_rcp_f32_e64 v76, v76 clamp
	v_rcp_f32_e64 v77, v77 clamp
	v_rcp_f32_e64 v78, v78 clamp
	v_rcp_f32_e64 v79, v79 clamp
	v_rcp_f32_e64 v80, v80 clamp
	v_rcp_f32_e64 v81, v81 clamp
	v_rcp_f32_e64 v82, v82 clamp
	v_rcp_f32_e64 v83, v83 clamp
	v_rcp_f32_e64 v52, v52 clamp
	v_rcp_f32_e64 v53, v53 clamp
	v_rcp_f32_e64 v26, v26 clamp
	v_rcp_f32_e64 v27, v27 clamp
	v_pk_mul_f32 v[52:53], v[54:55], v[52:53]
	v_pk_mul_f32 v[0:1], v[0:1], v[62:63]
	v_pk_mul_f32 v[44:45], v[44:45], v[64:65]
	v_pk_mul_f32 v[46:47], v[46:47], v[76:77]
	v_pk_mul_f32 v[56:57], v[56:57], v[78:79]
	v_pk_mul_f32 v[62:63], v[66:67], v[80:81]
	v_pk_mul_f32 v[64:65], v[74:75], v[82:83]
	v_pk_mul_f32 v[26:27], v[28:29], v[26:27]
	v_pk_fma_f32 v[18:19], v[18:19], v[52:53], v[52:53]
	v_pk_fma_f32 v[28:29], v[48:49], v[0:1], v[0:1]
	v_pk_fma_f32 v[48:49], v[50:51], v[44:45], v[44:45]
	v_pk_fma_f32 v[50:51], v[58:59], v[46:47], v[46:47]
	v_pk_fma_f32 v[54:55], v[60:61], v[56:57], v[56:57]
	v_pk_fma_f32 v[30:31], v[30:31], v[62:63], v[62:63]
	v_pk_fma_f32 v[32:33], v[32:33], v[64:65], v[64:65]
	v_pk_fma_f32 v[20:21], v[20:21], v[26:27], v[26:27]
	s_nop 0
	v_pk_fma_f32 v[28:29], v[28:29], v[28:29], s[4:5] neg_lo:[1,0,0] neg_hi:[1,0,0] clamp
	v_pk_fma_f32 v[48:49], v[48:49], v[48:49], s[4:5] neg_lo:[1,0,0] neg_hi:[1,0,0] clamp
	v_pk_fma_f32 v[50:51], v[50:51], v[50:51], s[4:5] neg_lo:[1,0,0] neg_hi:[1,0,0] clamp
	v_pk_fma_f32 v[54:55], v[54:55], v[54:55], s[4:5] neg_lo:[1,0,0] neg_hi:[1,0,0] clamp
	v_pk_fma_f32 v[30:31], v[30:31], v[30:31], s[4:5] neg_lo:[1,0,0] neg_hi:[1,0,0] clamp
	v_pk_fma_f32 v[32:33], v[32:33], v[32:33], s[4:5] neg_lo:[1,0,0] neg_hi:[1,0,0] clamp
	v_pk_fma_f32 v[18:19], v[18:19], v[18:19], s[4:5] neg_lo:[1,0,0] neg_hi:[1,0,0] clamp
	s_nop 0
	v_pk_fma_f32 v[20:21], v[20:21], v[20:21], s[4:5] neg_lo:[1,0,0] neg_hi:[1,0,0] clamp
	s_nop 0
	v_pk_fma_f32 v[28:29], v[28:29], v[28:29], s[8:9] op_sel_hi:[1,1,0]
	v_pk_fma_f32 v[48:49], v[48:49], v[48:49], s[8:9] op_sel_hi:[1,1,0]
	v_pk_fma_f32 v[50:51], v[50:51], v[50:51], s[8:9] op_sel_hi:[1,1,0]
	v_pk_fma_f32 v[54:55], v[54:55], v[54:55], s[8:9] op_sel_hi:[1,1,0]
	v_pk_fma_f32 v[30:31], v[30:31], v[30:31], s[8:9] op_sel_hi:[1,1,0]
	v_pk_fma_f32 v[32:33], v[32:33], v[32:33], s[8:9] op_sel_hi:[1,1,0]
	v_pk_fma_f32 v[18:19], v[18:19], v[18:19], s[8:9] op_sel_hi:[1,1,0]
	v_pk_fma_f32 v[20:21], v[20:21], v[20:21], s[8:9] op_sel_hi:[1,1,0]
	v_pk_mul_f32 v[0:1], v[0:1], v[28:29]
	v_pk_mul_f32 v[58:59], v[44:45], v[48:49]
	v_pk_mul_f32 v[60:61], v[46:47], v[50:51]
	v_pk_mul_f32 v[54:55], v[56:57], v[54:55]
	v_pk_mul_f32 v[62:63], v[62:63], v[30:31]
	v_pk_mul_f32 v[64:65], v[64:65], v[32:33]
	v_pk_mul_f32 v[66:67], v[18:19], v[52:53]
	v_pk_mul_f32 v[74:75], v[26:27], v[20:21]
	ds_read_b128 v[18:21], v72 offset:36864
	ds_read_b128 v[30:33], v72 offset:37888
	ds_read_b128 v[26:29], v71 offset:43520
	v_cvt_pk_f16_f32 v56, v60, v61
	v_cvt_pk_f16_f32 v57, v54, v55
	v_cvt_pk_f16_f32 v54, v62, v63
	ds_read_b128 v[60:63], v71 offset:43584
	v_cvt_pk_f16_f32 v52, v0, v1
	v_cvt_pk_f16_f32 v53, v58, v59
	s_waitcnt lgkmcnt(1)
	v_mfma_f32_16x16x32_f16 v[48:51], v[18:21], v[34:37], v[26:29]
	v_cvt_pk_f16_f32 v55, v64, v65
	v_cvt_pk_f16_f32 v58, v66, v67
	v_cvt_pk_f16_f32 v59, v74, v75
	v_mfma_f32_16x16x32_f16 v[18:21], v[18:21], v[22:25], v[26:29]
	ds_read_b128 v[44:47], v72 offset:40960
	s_add_i32 s12, s12, s3
	s_add_i32 s10, s20, s12
	v_mfma_f32_16x16x32_f16 v[26:29], v[30:33], v[52:55], v[48:51]
	s_cmp_lt_i32 s10, 0x8000
	v_add_u32_e32 v38, s7, v38
	s_nop 0
	ds_read_b128 v[48:51], v72 offset:38912
	v_mfma_f32_16x16x32_f16 v[18:21], v[30:33], v[56:59], v[18:21]
	ds_read_b128 v[30:33], v72 offset:39936
	s_nop 1
	v_cvt_pk_f16_f32 v1, v28, v29
	v_cvt_pk_f16_f32 v0, v26, v27
	s_waitcnt lgkmcnt(1)
	v_mfma_f32_16x16x32_f16 v[34:37], v[48:51], v[34:37], v[60:63]
	v_pk_max_f16 v27, v1, 0
	v_cvt_pk_f16_f32 v1, v20, v21
	v_pk_max_f16 v26, v0, 0
	v_mfma_f32_16x16x32_f16 v[20:23], v[48:51], v[22:25], v[60:63]
	v_cvt_pk_f16_f32 v0, v18, v19
	v_pk_max_f16 v18, v0, 0
	v_pk_max_f16 v19, v1, 0
	s_waitcnt lgkmcnt(0)
	v_mfma_f32_16x16x32_f16 v[34:37], v[30:33], v[52:55], v[34:37]
	v_mfma_f32_16x16x32_f16 v[20:23], v[30:33], v[56:59], v[20:23]
	s_nop 6
	v_cvt_pk_f16_f32 v0, v34, v35
	v_cvt_pk_f16_f32 v1, v36, v37
	v_pk_max_f16 v28, v0, 0
	v_pk_max_f16 v29, v1, 0
	v_cvt_pk_f16_f32 v0, v20, v21
	v_cvt_pk_f16_f32 v1, v22, v23
	v_pk_max_f16 v20, v0, 0
	v_pk_max_f16 v21, v1, 0
	v_mfma_f32_16x16x32_f16 v[24:27], v[44:47], v[26:29], 0
	s_nop 0
	v_mfma_f32_16x16x32_f16 v[18:21], v[44:47], v[18:21], 0
	s_nop 7
	v_cndmask_b32_e64 v18, v24, v18, s[0:1]
	s_cbranch_scc0 .LBB0_37

.Lprio_done:
	s_add_u32 s33, s33, 1
	s_cmp_lg_u32 s12, 0
	s_cselect_b64 s[10:11], -1, 0
	s_and_b64 s[16:17], s[10:11], vcc
	s_and_saveexec_b64 s[10:11], s[16:17]
	s_cbranch_execz .LBB0_34
	v_exp_f32_e32 v0, v18
	s_nop 0
	v_fma_f32 v0, v0, v70, 1.0
	v_rcp_f32_e32 v18, v0
	s_nop 0
	global_store_dword v38, v18, s[14:15]
	s_branch .LBB0_34
